# v10_reghandoff
# baseline (speedup 1.0000x reference)
.LBB1_98:
	s_mov_b32 s59, s56
	s_mov_b64 s[54:55], -1
	s_and_b64 vcc, exec, s[82:83]
	s_cmp_lg_u32 s59, 0
	s_cbranch_scc1 .Lskip_topbar_1
	s_waitcnt lgkmcnt(0)
	s_barrier

.LBB1_104:
	s_lshl_b32 s96, s59, 4
	v_or_b32_e32 v164, s96, v131
	s_andn2_b64 vcc, exec, s[54:55]
	v_lshlrev_b32_e32 v163, 2, v164
	s_cbranch_vccnz .LBB1_114
	v_or_b32_e32 v66, s96, v130
	v_mul_lo_u32 v165, v66, s95
	v_add3_u32 v68, v163, v165, s85
	s_cmp_eq_u32 s59, 0
	s_cbranch_scc1 .Lp1_lds_1
	v_accvgpr_read_b32 v66, a0
	v_accvgpr_read_b32 v67, a1
	v_accvgpr_read_b32 v68, a2
	v_accvgpr_read_b32 v69, a3
	s_branch .Lp1_go_1
.Lp1_lds_1:
	v_mov_b32_e32 v72, v68
	s_nop 0
	ds_read2_b32 v[66:67], v72 offset1:68
	ds_read2_b32 v[68:69], v72 offset0:136 offset1:204
	s_waitcnt lgkmcnt(0)
.Lp1_go_1:
	v_accvgpr_write_b32 a4, v137
	v_accvgpr_write_b32 a5, v138
	v_accvgpr_write_b32 a6, v139
	v_readlane_b32 s54, v66, 0
	v_accvgpr_write_b32 a7, v140
	v_cmp_lt_i32_e32 vcc, 0, v136
	v_rcp_f32_e64 v73, -s54
	v_writelane_b32 v166, s54, 0
	v_cndmask_b32_e64 v72, 0, v66, s[6:7]
	v_mul_f32_e32 v70, v72, v73
	s_nop 1
	v_mfma_f32_16x16x4_f32 v[66:69], v70, v66, v[66:69]
	v_mfma_f32_16x16x4_f32 a[4:7], v70, v137, a[4:7]
	s_nop 5
	v_readlane_b32 s54, v67, 1
	v_cndmask_b32_e64 v72, 0, v67, s[8:9]
	s_nop 0
	v_rcp_f32_e64 v73, -s54
	v_writelane_b32 v166, s54, 1
	v_mul_f32_e32 v71, v72, v73
	s_nop 1
	v_mfma_f32_16x16x4_f32 v[66:69], v71, v67, v[66:69]
	v_mfma_f32_16x16x4_f32 a[4:7], v71, a5, a[4:7]
	s_nop 5
	v_readlane_b32 s54, v68, 2
	v_cndmask_b32_e64 v72, 0, v68, s[10:11]
	s_nop 0
	v_rcp_f32_e64 v73, -s54
	v_writelane_b32 v166, s54, 2
	v_mul_f32_e32 v70, v72, v73
	s_nop 1
	v_mfma_f32_16x16x4_f32 v[66:69], v70, v68, v[66:69]
	v_mfma_f32_16x16x4_f32 a[4:7], v70, a6, a[4:7]
	s_nop 5
	v_readlane_b32 s54, v69, 3
	v_cndmask_b32_e64 v72, 0, v69, s[12:13]
	s_nop 0
	v_rcp_f32_e64 v73, -s54
	v_writelane_b32 v166, s54, 3
	v_mul_f32_e32 v71, v72, v73
	s_nop 1
	v_mfma_f32_16x16x4_f32 v[66:69], v71, v69, v[66:69]
	v_mfma_f32_16x16x4_f32 a[4:7], v71, a7, a[4:7]
	s_nop 5
	v_readlane_b32 s54, v66, 20
	v_cndmask_b32_e64 v72, 0, v66, s[14:15]
	s_nop 0
	v_rcp_f32_e64 v73, -s54
	v_writelane_b32 v166, s54, 4
	v_mul_f32_e32 v70, v72, v73
	s_nop 1
	v_mfma_f32_16x16x4_f32 v[66:69], v70, v66, v[66:69]
	v_mfma_f32_16x16x4_f32 a[4:7], v70, a4, a[4:7]
	s_nop 5
	v_readlane_b32 s54, v67, 21
	v_cndmask_b32_e64 v72, 0, v67, s[16:17]
	s_nop 0
	v_rcp_f32_e64 v73, -s54
	v_writelane_b32 v166, s54, 5
	v_mul_f32_e32 v71, v72, v73
	s_nop 1
	v_mfma_f32_16x16x4_f32 v[66:69], v71, v67, v[66:69]
	v_mfma_f32_16x16x4_f32 a[4:7], v71, a5, a[4:7]
	s_nop 5
	v_readlane_b32 s54, v68, 22
	v_cndmask_b32_e64 v72, 0, v68, s[18:19]
	s_nop 0
	v_rcp_f32_e64 v73, -s54
	v_writelane_b32 v166, s54, 6
	v_mul_f32_e32 v70, v72, v73
	s_nop 1
	v_mfma_f32_16x16x4_f32 v[66:69], v70, v68, v[66:69]
	v_mfma_f32_16x16x4_f32 a[4:7], v70, a6, a[4:7]
	s_nop 5
	v_readlane_b32 s54, v69, 23
	v_cndmask_b32_e64 v72, 0, v69, s[20:21]
	s_nop 0
	v_rcp_f32_e64 v73, -s54
	v_writelane_b32 v166, s54, 7
	v_mul_f32_e32 v71, v72, v73
	s_nop 1
	v_mfma_f32_16x16x4_f32 v[66:69], v71, v69, v[66:69]
	v_mfma_f32_16x16x4_f32 a[4:7], v71, a7, a[4:7]
	s_nop 5
	v_readlane_b32 s54, v66, 40
	v_cndmask_b32_e64 v72, 0, v66, s[22:23]
	s_nop 0
	v_rcp_f32_e64 v73, -s54
	v_writelane_b32 v166, s54, 8
	v_mul_f32_e32 v70, v72, v73
	s_nop 1
	v_mfma_f32_16x16x4_f32 v[66:69], v70, v66, v[66:69]
	v_mfma_f32_16x16x4_f32 a[4:7], v70, a4, a[4:7]
	s_nop 5
	v_readlane_b32 s54, v67, 41
	v_cndmask_b32_e64 v72, 0, v67, s[24:25]
	s_nop 0
	v_rcp_f32_e64 v73, -s54
	v_writelane_b32 v166, s54, 9
	v_mul_f32_e32 v71, v72, v73
	s_nop 1
	v_mfma_f32_16x16x4_f32 v[66:69], v71, v67, v[66:69]
	v_mfma_f32_16x16x4_f32 a[4:7], v71, a5, a[4:7]
	s_nop 5
	v_readlane_b32 s54, v68, 42
	v_cndmask_b32_e64 v72, 0, v68, s[26:27]
	s_nop 0
	v_rcp_f32_e64 v73, -s54
	v_writelane_b32 v166, s54, 10
	v_mul_f32_e32 v70, v72, v73
	s_nop 1
	v_mfma_f32_16x16x4_f32 v[66:69], v70, v68, v[66:69]
	v_mfma_f32_16x16x4_f32 a[4:7], v70, a6, a[4:7]
	s_nop 5
	v_readlane_b32 s54, v69, 43
	v_cndmask_b32_e64 v72, 0, v69, s[28:29]
	s_nop 0
	v_rcp_f32_e64 v73, -s54
	v_writelane_b32 v166, s54, 11
	v_mul_f32_e32 v71, v72, v73
	s_nop 1
	v_mfma_f32_16x16x4_f32 v[66:69], v71, v69, v[66:69]
	v_mfma_f32_16x16x4_f32 a[4:7], v71, a7, a[4:7]
	s_nop 5
	v_readlane_b32 s54, v66, 60
	v_cndmask_b32_e64 v72, 0, v66, s[30:31]
	s_nop 0
	v_rcp_f32_e64 v73, -s54
	v_writelane_b32 v166, s54, 12
	v_mul_f32_e32 v70, v72, v73
	s_nop 1
	v_mfma_f32_16x16x4_f32 v[66:69], v70, v66, v[66:69]
	v_mfma_f32_16x16x4_f32 a[4:7], v70, a4, a[4:7]
	s_nop 5
	v_readlane_b32 s54, v67, 61
	v_cndmask_b32_e64 v72, 0, v67, s[34:35]
	s_nop 0
	v_rcp_f32_e64 v73, -s54
	v_writelane_b32 v166, s54, 13
	v_mul_f32_e32 v71, v72, v73
	s_nop 1
	v_mfma_f32_16x16x4_f32 v[66:69], v71, v67, v[66:69]
	v_mfma_f32_16x16x4_f32 a[4:7], v71, a5, a[4:7]
	s_nop 5
	v_readlane_b32 s54, v68, 62
	v_cndmask_b32_e64 v72, 0, v68, s[36:37]
	s_nop 0
	v_rcp_f32_e64 v73, -s54
	v_writelane_b32 v166, s54, 14
	v_mul_f32_e32 v70, v72, v73
	s_nop 1
	v_mfma_f32_16x16x4_f32 v[66:69], v70, v68, v[66:69]
	v_mfma_f32_16x16x4_f32 a[4:7], v70, a6, a[4:7]
	s_nop 5
	v_readlane_b32 s54, v69, 63
	s_nop 2
	v_writelane_b32 v166, s54, 15
	v_accvgpr_read_b32 v73, a7
	v_accvgpr_read_b32 v72, a6
	v_accvgpr_read_b32 v71, a5
	v_accvgpr_read_b32 v70, a4
	s_and_saveexec_b64 s[54:55], s[4:5]
	s_cbranch_execz .LBB1_113
	s_waitcnt lgkmcnt(2)
	v_lshl_add_u32 v167, s96, 2, v134
	ds_write_b32 v167, v166

.LBB1_219:
	s_mov_b32 s59, s56
	s_mov_b64 s[52:53], -1
	s_and_b64 vcc, exec, s[82:83]
	s_cmp_lg_u32 s59, 0
	s_cbranch_scc1 .Lskip_topbar_2
	s_waitcnt lgkmcnt(0)
	s_barrier

.LBB1_225:
	s_lshl_b32 s97, s59, 4
	v_or_b32_e32 v14, s97, v131
	s_andn2_b64 vcc, exec, s[52:53]
	v_lshlrev_b32_e32 v13, 2, v14
	s_cbranch_vccnz .LBB1_235
	v_or_b32_e32 v2, s97, v130
	v_mul_lo_u32 v15, v2, s57
	v_add3_u32 v4, v13, v15, s95
	s_cmp_eq_u32 s59, 0
	s_cbranch_scc1 .Lp1_lds_2
	v_accvgpr_read_b32 v2, a0
	v_accvgpr_read_b32 v3, a1
	v_accvgpr_read_b32 v4, a2
	v_accvgpr_read_b32 v5, a3
	s_branch .Lp1_go_2
.Lp1_lds_2:
	v_mov_b32_e32 v8, v4
	s_nop 0
	ds_read2_b32 v[2:3], v8 offset1:68
	ds_read2_b32 v[4:5], v8 offset0:136 offset1:204
	s_waitcnt lgkmcnt(0)
.Lp1_go_2:
	v_accvgpr_write_b32 a4, v137
	v_accvgpr_write_b32 a5, v138
	v_accvgpr_write_b32 a6, v139
	v_readlane_b32 s52, v2, 0
	v_accvgpr_write_b32 a7, v140
	v_cmp_lt_i32_e32 vcc, 0, v136
	v_rcp_f32_e64 v9, -s52
	v_writelane_b32 v16, s52, 0
	v_cndmask_b32_e64 v8, 0, v2, s[6:7]
	v_mul_f32_e32 v6, v8, v9
	s_nop 1
	v_mfma_f32_16x16x4_f32 v[2:5], v6, v2, v[2:5]
	v_mfma_f32_16x16x4_f32 a[4:7], v6, v137, a[4:7]
	s_nop 5
	v_readlane_b32 s52, v3, 1
	v_cndmask_b32_e64 v8, 0, v3, s[8:9]
	s_nop 0
	v_rcp_f32_e64 v9, -s52
	v_writelane_b32 v16, s52, 1
	v_mul_f32_e32 v7, v8, v9
	s_nop 1
	v_mfma_f32_16x16x4_f32 v[2:5], v7, v3, v[2:5]
	v_mfma_f32_16x16x4_f32 a[4:7], v7, a5, a[4:7]
	s_nop 5
	v_readlane_b32 s52, v4, 2
	v_cndmask_b32_e64 v8, 0, v4, s[10:11]
	s_nop 0
	v_rcp_f32_e64 v9, -s52
	v_writelane_b32 v16, s52, 2
	v_mul_f32_e32 v6, v8, v9
	s_nop 1
	v_mfma_f32_16x16x4_f32 v[2:5], v6, v4, v[2:5]
	v_mfma_f32_16x16x4_f32 a[4:7], v6, a6, a[4:7]
	s_nop 5
	v_readlane_b32 s52, v5, 3
	v_cndmask_b32_e64 v8, 0, v5, s[12:13]
	s_nop 0
	v_rcp_f32_e64 v9, -s52
	v_writelane_b32 v16, s52, 3
	v_mul_f32_e32 v7, v8, v9
	s_nop 1
	v_mfma_f32_16x16x4_f32 v[2:5], v7, v5, v[2:5]
	v_mfma_f32_16x16x4_f32 a[4:7], v7, a7, a[4:7]
	s_nop 5
	v_readlane_b32 s52, v2, 20
	v_cndmask_b32_e64 v8, 0, v2, s[14:15]
	s_nop 0
	v_rcp_f32_e64 v9, -s52
	v_writelane_b32 v16, s52, 4
	v_mul_f32_e32 v6, v8, v9
	s_nop 1
	v_mfma_f32_16x16x4_f32 v[2:5], v6, v2, v[2:5]
	v_mfma_f32_16x16x4_f32 a[4:7], v6, a4, a[4:7]
	s_nop 5
	v_readlane_b32 s52, v3, 21
	v_cndmask_b32_e64 v8, 0, v3, s[16:17]
	s_nop 0
	v_rcp_f32_e64 v9, -s52
	v_writelane_b32 v16, s52, 5
	v_mul_f32_e32 v7, v8, v9
	s_nop 1
	v_mfma_f32_16x16x4_f32 v[2:5], v7, v3, v[2:5]
	v_mfma_f32_16x16x4_f32 a[4:7], v7, a5, a[4:7]
	s_nop 5
	v_readlane_b32 s52, v4, 22
	v_cndmask_b32_e64 v8, 0, v4, s[18:19]
	s_nop 0
	v_rcp_f32_e64 v9, -s52
	v_writelane_b32 v16, s52, 6
	v_mul_f32_e32 v6, v8, v9
	s_nop 1
	v_mfma_f32_16x16x4_f32 v[2:5], v6, v4, v[2:5]
	v_mfma_f32_16x16x4_f32 a[4:7], v6, a6, a[4:7]
	s_nop 5
	v_readlane_b32 s52, v5, 23
	v_cndmask_b32_e64 v8, 0, v5, s[20:21]
	s_nop 0
	v_rcp_f32_e64 v9, -s52
	v_writelane_b32 v16, s52, 7
	v_mul_f32_e32 v7, v8, v9
	s_nop 1
	v_mfma_f32_16x16x4_f32 v[2:5], v7, v5, v[2:5]
	v_mfma_f32_16x16x4_f32 a[4:7], v7, a7, a[4:7]
	s_nop 5
	v_readlane_b32 s52, v2, 40
	v_cndmask_b32_e64 v8, 0, v2, s[22:23]
	s_nop 0
	v_rcp_f32_e64 v9, -s52
	v_writelane_b32 v16, s52, 8
	v_mul_f32_e32 v6, v8, v9
	s_nop 1
	v_mfma_f32_16x16x4_f32 v[2:5], v6, v2, v[2:5]
	v_mfma_f32_16x16x4_f32 a[4:7], v6, a4, a[4:7]
	s_nop 5
	v_readlane_b32 s52, v3, 41
	v_cndmask_b32_e64 v8, 0, v3, s[24:25]
	s_nop 0
	v_rcp_f32_e64 v9, -s52
	v_writelane_b32 v16, s52, 9
	v_mul_f32_e32 v7, v8, v9
	s_nop 1
	v_mfma_f32_16x16x4_f32 v[2:5], v7, v3, v[2:5]
	v_mfma_f32_16x16x4_f32 a[4:7], v7, a5, a[4:7]
	s_nop 5
	v_readlane_b32 s52, v4, 42
	v_cndmask_b32_e64 v8, 0, v4, s[26:27]
	s_nop 0
	v_rcp_f32_e64 v9, -s52
	v_writelane_b32 v16, s52, 10
	v_mul_f32_e32 v6, v8, v9
	s_nop 1
	v_mfma_f32_16x16x4_f32 v[2:5], v6, v4, v[2:5]
	v_mfma_f32_16x16x4_f32 a[4:7], v6, a6, a[4:7]
	s_nop 5
	v_readlane_b32 s52, v5, 43
	v_cndmask_b32_e64 v8, 0, v5, s[28:29]
	s_nop 0
	v_rcp_f32_e64 v9, -s52
	v_writelane_b32 v16, s52, 11
	v_mul_f32_e32 v7, v8, v9
	s_nop 1
	v_mfma_f32_16x16x4_f32 v[2:5], v7, v5, v[2:5]
	v_mfma_f32_16x16x4_f32 a[4:7], v7, a7, a[4:7]
	s_nop 5
	v_readlane_b32 s52, v2, 60
	v_cndmask_b32_e64 v8, 0, v2, s[30:31]
	s_nop 0
	v_rcp_f32_e64 v9, -s52
	v_writelane_b32 v16, s52, 12
	v_mul_f32_e32 v6, v8, v9
	s_nop 1
	v_mfma_f32_16x16x4_f32 v[2:5], v6, v2, v[2:5]
	v_mfma_f32_16x16x4_f32 a[4:7], v6, a4, a[4:7]
	s_nop 5
	v_readlane_b32 s52, v3, 61
	v_cndmask_b32_e64 v8, 0, v3, s[34:35]
	s_nop 0
	v_rcp_f32_e64 v9, -s52
	v_writelane_b32 v16, s52, 13
	v_mul_f32_e32 v7, v8, v9
	s_nop 1
	v_mfma_f32_16x16x4_f32 v[2:5], v7, v3, v[2:5]
	v_mfma_f32_16x16x4_f32 a[4:7], v7, a5, a[4:7]
	s_nop 5
	v_readlane_b32 s52, v4, 62
	v_cndmask_b32_e64 v8, 0, v4, s[36:37]
	s_nop 0
	v_rcp_f32_e64 v9, -s52
	v_writelane_b32 v16, s52, 14
	v_mul_f32_e32 v6, v8, v9
	s_nop 1
	v_mfma_f32_16x16x4_f32 v[2:5], v6, v4, v[2:5]
	v_mfma_f32_16x16x4_f32 a[4:7], v6, a6, a[4:7]
	s_nop 5
	v_readlane_b32 s52, v5, 63
	s_nop 2
	v_writelane_b32 v16, s52, 15
	v_accvgpr_read_b32 v9, a7
	v_accvgpr_read_b32 v8, a6
	v_accvgpr_read_b32 v7, a5
	v_accvgpr_read_b32 v6, a4
	s_and_saveexec_b64 s[52:53], s[4:5]
	s_cbranch_execz .LBB1_234
	s_waitcnt lgkmcnt(2)
	v_lshl_add_u32 v17, s97, 2, v134
	ds_write_b32 v17, v16

.LBB1_289:
	s_mov_b32 s79, s52
	s_mov_b64 s[52:53], -1
	s_and_b64 vcc, exec, s[56:57]
	s_cmp_lg_u32 s79, 0
	s_cbranch_scc1 .Lskip_topbar_3
	s_waitcnt lgkmcnt(0)
	s_barrier

.LBB1_295:
	s_lshl_b32 s80, s79, 4
	v_or_b32_e32 v42, s80, v19
	s_andn2_b64 vcc, exec, s[52:53]
	v_lshlrev_b32_e32 v41, 2, v42
	s_cbranch_vccnz .LBB1_305
	v_or_b32_e32 v2, s80, v18
	v_mul_lo_u32 v44, v2, s78
	v_add3_u32 v4, v41, v44, s69
	s_cmp_eq_u32 s79, 0
	s_cbranch_scc1 .Lp1_lds_3
	v_accvgpr_read_b32 v2, a0
	v_accvgpr_read_b32 v3, a1
	v_accvgpr_read_b32 v4, a2
	v_accvgpr_read_b32 v5, a3
	s_branch .Lp1_go_3

.Lp1_go_3:
	v_accvgpr_write_b32 a4, v22
	v_accvgpr_write_b32 a5, v23
	v_accvgpr_write_b32 a6, v24
	v_readlane_b32 s52, v2, 0
	v_accvgpr_write_b32 a7, v25
	v_cmp_lt_i32_e32 vcc, 0, v21
	v_rcp_f32_e64 v9, -s52
	v_writelane_b32 v53, s52, 0
	v_cndmask_b32_e64 v8, 0, v2, s[4:5]
	v_mul_f32_e32 v6, v8, v9
	s_nop 1
	v_mfma_f32_16x16x4_f32 v[2:5], v6, v2, v[2:5]
	v_mfma_f32_16x16x4_f32 a[4:7], v6, v22, a[4:7]
	s_nop 5
	v_readlane_b32 s52, v3, 1
	v_cndmask_b32_e64 v8, 0, v3, s[6:7]
	s_nop 0
	v_rcp_f32_e64 v9, -s52
	v_writelane_b32 v53, s52, 1
	v_mul_f32_e32 v7, v8, v9
	s_nop 1
	v_mfma_f32_16x16x4_f32 v[2:5], v7, v3, v[2:5]
	v_mfma_f32_16x16x4_f32 a[4:7], v7, a5, a[4:7]
	s_nop 5
	v_readlane_b32 s52, v4, 2
	v_cndmask_b32_e64 v8, 0, v4, s[8:9]
	s_nop 0
	v_rcp_f32_e64 v9, -s52
	v_writelane_b32 v53, s52, 2
	v_mul_f32_e32 v6, v8, v9
	s_nop 1
	v_mfma_f32_16x16x4_f32 v[2:5], v6, v4, v[2:5]
	v_mfma_f32_16x16x4_f32 a[4:7], v6, a6, a[4:7]
	s_nop 5
	v_readlane_b32 s52, v5, 3
	v_cndmask_b32_e64 v8, 0, v5, s[10:11]
	s_nop 0
	v_rcp_f32_e64 v9, -s52
	v_writelane_b32 v53, s52, 3
	v_mul_f32_e32 v7, v8, v9
	s_nop 1
	v_mfma_f32_16x16x4_f32 v[2:5], v7, v5, v[2:5]
	v_mfma_f32_16x16x4_f32 a[4:7], v7, a7, a[4:7]
	s_nop 5
	v_readlane_b32 s52, v2, 20
	v_cndmask_b32_e64 v8, 0, v2, s[12:13]
	s_nop 0
	v_rcp_f32_e64 v9, -s52
	v_writelane_b32 v53, s52, 4
	v_mul_f32_e32 v6, v8, v9
	s_nop 1
	v_mfma_f32_16x16x4_f32 v[2:5], v6, v2, v[2:5]
	v_mfma_f32_16x16x4_f32 a[4:7], v6, a4, a[4:7]
	s_nop 5
	v_readlane_b32 s52, v3, 21
	v_cndmask_b32_e64 v8, 0, v3, s[14:15]
	s_nop 0
	v_rcp_f32_e64 v9, -s52
	v_writelane_b32 v53, s52, 5
	v_mul_f32_e32 v7, v8, v9
	s_nop 1
	v_mfma_f32_16x16x4_f32 v[2:5], v7, v3, v[2:5]
	v_mfma_f32_16x16x4_f32 a[4:7], v7, a5, a[4:7]
	s_nop 5
	v_readlane_b32 s52, v4, 22
	v_cndmask_b32_e64 v8, 0, v4, s[16:17]
	s_nop 0
	v_rcp_f32_e64 v9, -s52
	v_writelane_b32 v53, s52, 6
	v_mul_f32_e32 v6, v8, v9
	s_nop 1
	v_mfma_f32_16x16x4_f32 v[2:5], v6, v4, v[2:5]
	v_mfma_f32_16x16x4_f32 a[4:7], v6, a6, a[4:7]
	s_nop 5
	v_readlane_b32 s52, v5, 23
	v_cndmask_b32_e64 v8, 0, v5, s[18:19]
	s_nop 0
	v_rcp_f32_e64 v9, -s52
	v_writelane_b32 v53, s52, 7
	v_mul_f32_e32 v7, v8, v9
	s_nop 1
	v_mfma_f32_16x16x4_f32 v[2:5], v7, v5, v[2:5]
	v_mfma_f32_16x16x4_f32 a[4:7], v7, a7, a[4:7]
	s_nop 5
	v_readlane_b32 s52, v2, 40
	v_cndmask_b32_e64 v8, 0, v2, s[20:21]
	s_nop 0
	v_rcp_f32_e64 v9, -s52
	v_writelane_b32 v53, s52, 8
	v_mul_f32_e32 v6, v8, v9
	s_nop 1
	v_mfma_f32_16x16x4_f32 v[2:5], v6, v2, v[2:5]
	v_mfma_f32_16x16x4_f32 a[4:7], v6, a4, a[4:7]
	s_nop 5
	v_readlane_b32 s52, v3, 41
	v_cndmask_b32_e64 v8, 0, v3, s[22:23]
	s_nop 0
	v_rcp_f32_e64 v9, -s52
	v_writelane_b32 v53, s52, 9
	v_mul_f32_e32 v7, v8, v9
	s_nop 1
	v_mfma_f32_16x16x4_f32 v[2:5], v7, v3, v[2:5]
	v_mfma_f32_16x16x4_f32 a[4:7], v7, a5, a[4:7]
	s_nop 5
	v_readlane_b32 s52, v4, 42
	v_cndmask_b32_e64 v8, 0, v4, s[24:25]
	s_nop 0
	v_rcp_f32_e64 v9, -s52
	v_writelane_b32 v53, s52, 10
	v_mul_f32_e32 v6, v8, v9
	s_nop 1
	v_mfma_f32_16x16x4_f32 v[2:5], v6, v4, v[2:5]
	v_mfma_f32_16x16x4_f32 a[4:7], v6, a6, a[4:7]
	s_nop 5
	v_readlane_b32 s52, v5, 43
	v_cndmask_b32_e64 v8, 0, v5, s[26:27]
	s_nop 0
	v_rcp_f32_e64 v9, -s52
	v_writelane_b32 v53, s52, 11
	v_mul_f32_e32 v7, v8, v9
	s_nop 1
	v_mfma_f32_16x16x4_f32 v[2:5], v7, v5, v[2:5]
	v_mfma_f32_16x16x4_f32 a[4:7], v7, a7, a[4:7]
	s_nop 5
	v_readlane_b32 s52, v2, 60
	v_cndmask_b32_e64 v8, 0, v2, s[28:29]
	s_nop 0
	v_rcp_f32_e64 v9, -s52
	v_writelane_b32 v53, s52, 12
	v_mul_f32_e32 v6, v8, v9
	s_nop 1
	v_mfma_f32_16x16x4_f32 v[2:5], v6, v2, v[2:5]
	v_mfma_f32_16x16x4_f32 a[4:7], v6, a4, a[4:7]
	s_nop 5
	v_readlane_b32 s52, v3, 61
	v_cndmask_b32_e64 v8, 0, v3, s[30:31]
	s_nop 0
	v_rcp_f32_e64 v9, -s52
	v_writelane_b32 v53, s52, 13
	v_mul_f32_e32 v7, v8, v9
	s_nop 1
	v_mfma_f32_16x16x4_f32 v[2:5], v7, v3, v[2:5]
	v_mfma_f32_16x16x4_f32 a[4:7], v7, a5, a[4:7]
	s_nop 5
	v_readlane_b32 s52, v4, 62
	v_cndmask_b32_e64 v8, 0, v4, s[34:35]
	s_nop 0
	v_rcp_f32_e64 v9, -s52
	v_writelane_b32 v53, s52, 14
	v_mul_f32_e32 v6, v8, v9
	s_nop 1
	v_mfma_f32_16x16x4_f32 v[2:5], v6, v4, v[2:5]
	v_mfma_f32_16x16x4_f32 a[4:7], v6, a6, a[4:7]
	s_nop 5
	v_readlane_b32 s52, v5, 63
	s_nop 2
	v_writelane_b32 v53, s52, 15
	v_accvgpr_read_b32 v9, a7
	v_accvgpr_read_b32 v8, a6
	v_accvgpr_read_b32 v7, a5
	v_accvgpr_read_b32 v6, a4
	s_and_saveexec_b64 s[52:53], s[2:3]
	s_cbranch_execz .LBB1_304
	s_waitcnt lgkmcnt(2)
	v_lshl_add_u32 v54, s80, 2, v11
	ds_write_b32 v54, v53

.LBB1_330:
	s_mov_b32 s74, s52
	s_mov_b64 s[52:53], -1
	s_and_b64 vcc, exec, s[56:57]
	s_cmp_lg_u32 s74, 0
	s_cbranch_scc1 .Lskip_topbar_4
	s_waitcnt lgkmcnt(0)
	s_barrier

.LBB1_336:
	s_lshl_b32 s75, s74, 4
	v_or_b32_e32 v34, s75, v19
	s_andn2_b64 vcc, exec, s[52:53]
	v_lshlrev_b32_e32 v14, 2, v34
	s_cbranch_vccnz .LBB1_346
	v_or_b32_e32 v0, s75, v18
	v_mul_lo_u32 v35, v0, s64
	v_add3_u32 v2, v14, v35, s72
	s_cmp_eq_u32 s74, 0
	s_cbranch_scc1 .Lp1_lds_4
	v_accvgpr_read_b32 v0, a0
	v_accvgpr_read_b32 v1, a1
	v_accvgpr_read_b32 v2, a2
	v_accvgpr_read_b32 v3, a3
	s_branch .Lp1_go_4
.Lp1_lds_4:
	v_mov_b32_e32 v6, v2
	s_nop 0
	ds_read2_b32 v[0:1], v6 offset1:68
	ds_read2_b32 v[2:3], v6 offset0:136 offset1:204
	s_waitcnt lgkmcnt(0)
.Lp1_go_4:
	v_accvgpr_write_b32 a4, v22
	v_accvgpr_write_b32 a5, v23
	v_accvgpr_write_b32 a6, v24
	v_readlane_b32 s52, v0, 0
	v_accvgpr_write_b32 a7, v25
	v_cmp_lt_i32_e32 vcc, 0, v21
	v_rcp_f32_e64 v7, -s52
	v_writelane_b32 v36, s52, 0
	v_cndmask_b32_e64 v6, 0, v0, s[4:5]
	v_mul_f32_e32 v4, v6, v7
	s_nop 1
	v_mfma_f32_16x16x4_f32 v[0:3], v4, v0, v[0:3]
	v_mfma_f32_16x16x4_f32 a[4:7], v4, v22, a[4:7]
	s_nop 5
	v_readlane_b32 s52, v1, 1
	v_cndmask_b32_e64 v6, 0, v1, s[6:7]
	s_nop 0
	v_rcp_f32_e64 v7, -s52
	v_writelane_b32 v36, s52, 1
	v_mul_f32_e32 v5, v6, v7
	s_nop 1
	v_mfma_f32_16x16x4_f32 v[0:3], v5, v1, v[0:3]
	v_mfma_f32_16x16x4_f32 a[4:7], v5, a5, a[4:7]
	s_nop 5
	v_readlane_b32 s52, v2, 2
	v_cndmask_b32_e64 v6, 0, v2, s[8:9]
	s_nop 0
	v_rcp_f32_e64 v7, -s52
	v_writelane_b32 v36, s52, 2
	v_mul_f32_e32 v4, v6, v7
	s_nop 1
	v_mfma_f32_16x16x4_f32 v[0:3], v4, v2, v[0:3]
	v_mfma_f32_16x16x4_f32 a[4:7], v4, a6, a[4:7]
	s_nop 5
	v_readlane_b32 s52, v3, 3
	v_cndmask_b32_e64 v6, 0, v3, s[10:11]
	s_nop 0
	v_rcp_f32_e64 v7, -s52
	v_writelane_b32 v36, s52, 3
	v_mul_f32_e32 v5, v6, v7
	s_nop 1
	v_mfma_f32_16x16x4_f32 v[0:3], v5, v3, v[0:3]
	v_mfma_f32_16x16x4_f32 a[4:7], v5, a7, a[4:7]
	s_nop 5
	v_readlane_b32 s52, v0, 20
	v_cndmask_b32_e64 v6, 0, v0, s[12:13]
	s_nop 0
	v_rcp_f32_e64 v7, -s52
	v_writelane_b32 v36, s52, 4
	v_mul_f32_e32 v4, v6, v7
	s_nop 1
	v_mfma_f32_16x16x4_f32 v[0:3], v4, v0, v[0:3]
	v_mfma_f32_16x16x4_f32 a[4:7], v4, a4, a[4:7]
	s_nop 5
	v_readlane_b32 s52, v1, 21
	v_cndmask_b32_e64 v6, 0, v1, s[14:15]
	s_nop 0
	v_rcp_f32_e64 v7, -s52
	v_writelane_b32 v36, s52, 5
	v_mul_f32_e32 v5, v6, v7
	s_nop 1
	v_mfma_f32_16x16x4_f32 v[0:3], v5, v1, v[0:3]
	v_mfma_f32_16x16x4_f32 a[4:7], v5, a5, a[4:7]
	s_nop 5
	v_readlane_b32 s52, v2, 22
	v_cndmask_b32_e64 v6, 0, v2, s[16:17]
	s_nop 0
	v_rcp_f32_e64 v7, -s52
	v_writelane_b32 v36, s52, 6
	v_mul_f32_e32 v4, v6, v7
	s_nop 1
	v_mfma_f32_16x16x4_f32 v[0:3], v4, v2, v[0:3]
	v_mfma_f32_16x16x4_f32 a[4:7], v4, a6, a[4:7]
	s_nop 5
	v_readlane_b32 s52, v3, 23
	v_cndmask_b32_e64 v6, 0, v3, s[18:19]
	s_nop 0
	v_rcp_f32_e64 v7, -s52
	v_writelane_b32 v36, s52, 7
	v_mul_f32_e32 v5, v6, v7
	s_nop 1
	v_mfma_f32_16x16x4_f32 v[0:3], v5, v3, v[0:3]
	v_mfma_f32_16x16x4_f32 a[4:7], v5, a7, a[4:7]
	s_nop 5
	v_readlane_b32 s52, v0, 40
	v_cndmask_b32_e64 v6, 0, v0, s[20:21]
	s_nop 0
	v_rcp_f32_e64 v7, -s52
	v_writelane_b32 v36, s52, 8
	v_mul_f32_e32 v4, v6, v7
	s_nop 1
	v_mfma_f32_16x16x4_f32 v[0:3], v4, v0, v[0:3]
	v_mfma_f32_16x16x4_f32 a[4:7], v4, a4, a[4:7]
	s_nop 5
	v_readlane_b32 s52, v1, 41
	v_cndmask_b32_e64 v6, 0, v1, s[22:23]
	s_nop 0
	v_rcp_f32_e64 v7, -s52
	v_writelane_b32 v36, s52, 9
	v_mul_f32_e32 v5, v6, v7
	s_nop 1
	v_mfma_f32_16x16x4_f32 v[0:3], v5, v1, v[0:3]
	v_mfma_f32_16x16x4_f32 a[4:7], v5, a5, a[4:7]
	s_nop 5
	v_readlane_b32 s52, v2, 42
	v_cndmask_b32_e64 v6, 0, v2, s[24:25]
	s_nop 0
	v_rcp_f32_e64 v7, -s52
	v_writelane_b32 v36, s52, 10
	v_mul_f32_e32 v4, v6, v7
	s_nop 1
	v_mfma_f32_16x16x4_f32 v[0:3], v4, v2, v[0:3]
	v_mfma_f32_16x16x4_f32 a[4:7], v4, a6, a[4:7]
	s_nop 5
	v_readlane_b32 s52, v3, 43
	v_cndmask_b32_e64 v6, 0, v3, s[26:27]
	s_nop 0
	v_rcp_f32_e64 v7, -s52
	v_writelane_b32 v36, s52, 11
	v_mul_f32_e32 v5, v6, v7
	s_nop 1
	v_mfma_f32_16x16x4_f32 v[0:3], v5, v3, v[0:3]
	v_mfma_f32_16x16x4_f32 a[4:7], v5, a7, a[4:7]
	s_nop 5
	v_readlane_b32 s52, v0, 60
	v_cndmask_b32_e64 v6, 0, v0, s[28:29]
	s_nop 0
	v_rcp_f32_e64 v7, -s52
	v_writelane_b32 v36, s52, 12
	v_mul_f32_e32 v4, v6, v7
	s_nop 1
	v_mfma_f32_16x16x4_f32 v[0:3], v4, v0, v[0:3]
	v_mfma_f32_16x16x4_f32 a[4:7], v4, a4, a[4:7]
	s_nop 5
	v_readlane_b32 s52, v1, 61
	v_cndmask_b32_e64 v6, 0, v1, s[30:31]
	s_nop 0
	v_rcp_f32_e64 v7, -s52
	v_writelane_b32 v36, s52, 13
	v_mul_f32_e32 v5, v6, v7
	s_nop 1
	v_mfma_f32_16x16x4_f32 v[0:3], v5, v1, v[0:3]
	v_mfma_f32_16x16x4_f32 a[4:7], v5, a5, a[4:7]
	s_nop 5
	v_readlane_b32 s52, v2, 62
	v_cndmask_b32_e64 v6, 0, v2, s[34:35]
	s_nop 0
	v_rcp_f32_e64 v7, -s52
	v_writelane_b32 v36, s52, 14
	v_mul_f32_e32 v4, v6, v7
	s_nop 1
	v_mfma_f32_16x16x4_f32 v[0:3], v4, v2, v[0:3]
	v_mfma_f32_16x16x4_f32 a[4:7], v4, a6, a[4:7]
	s_nop 5
	v_readlane_b32 s52, v3, 63
	s_nop 2
	v_writelane_b32 v36, s52, 15
	v_accvgpr_read_b32 v7, a7
	v_accvgpr_read_b32 v6, a6
	v_accvgpr_read_b32 v5, a5
	v_accvgpr_read_b32 v4, a4
	s_and_saveexec_b64 s[52:53], s[2:3]
	s_cbranch_execz .LBB1_345
	s_waitcnt lgkmcnt(2)
	v_lshl_add_u32 v37, s75, 2, v11
	ds_write_b32 v37, v36
